# baseline (speedup 1.0000x reference)
_Z9gemm_gldsILi256ELi192ELi4ELi2ELi2ELi4ELi8ELi0ELi4096ELi3072ELi1024EEvPKDF16_S1_PfPKfS4_PKiPDF16_S7_S7_:
	s_ashr_i32 s3, s2, 3
	s_lshr_b32 s9, s3, 30
	s_add_i32 s9, s3, s9
	s_lshl_b32 s8, s2, 1
	s_ashr_i32 s10, s9, 2
	s_and_b32 s9, s9, 0xfffffc
	s_lshl_b32 s2, s2, 3
	s_load_dwordx4 s[4:7], s[0:1], 0x0
	s_and_b32 s8, s8, 12
	s_sub_i32 s3, s3, s9
	s_and_b32 s20, s2, 8
	s_add_i32 s8, s8, s3
	s_add_i32 s20, s20, s10
	s_lshl_b32 s16, s8, 8
	s_mul_i32 s2, s20, 0xc0
	v_lshlrev_b32_e32 v139, 4, v0
	v_and_b32_e32 v1, 32, v0
	s_ashr_i32 s17, s16, 31
	s_ashr_i32 s3, s2, 31
	v_lshrrev_b32_e32 v2, 3, v0
	v_bfe_u32 v46, v0, 2, 4
	v_bitop3_b32 v1, v139, v1, 48 bitop3:0x6c
	s_lshl_b64 s[8:9], s[16:17], 11
	s_lshl_b64 s[10:11], s[2:3], 11
	v_and_or_b32 v2, v2, 48, v46
	v_and_or_b32 v47, v0, 64, v1
	s_waitcnt lgkmcnt(0)
	s_add_u32 s2, s4, s8
	s_addc_u32 s3, s5, s9
	v_lshl_or_b32 v2, v2, 11, v47
	v_lshrrev_b32_e32 v216, 3, v0
	v_and_b32_e32 v217, 7, v216
	v_and_b32_e32 v218, 7, v0
	v_xor_b32_e32 v217, v218, v217
	v_lshlrev_b32_e32 v217, 4, v217
	v_lshl_or_b32 v216, v216, 11, v217
	v_mov_b32_e32 v218, v2
	v_mov_b32_e32 v219, 0
	v_mov_b32_e32 v2, v216
	v_add_u32_e32 v194, 0x100, v2
	v_add_u32_e32 v195, 0x100, v218
	v_mov_b32_e32 v3, 0
	v_readfirstlane_b32 s4, v139
	v_or_b32_e32 v1, 0x2000, v139
	s_add_u32 s18, s6, s10
	v_lshl_add_u64 v[4:5], s[2:3], 0, v[2:3]
	s_mov_b32 m0, s4
	s_mov_b64 s[4:5], 0x20000
	v_readfirstlane_b32 s6, v1
	v_or_b32_e32 v1, 0x4000, v139
	s_addc_u32 s19, s7, s11
	v_readfirstlane_b32 s45, v139
	s_mov_b64 s[24:25], s[2:3]
	s_add_u32 s26, s2, 0x20000
	s_addc_u32 s27, s3, 0
	s_add_u32 s28, s2, 0x40000
	s_addc_u32 s29, s3, 0
	s_add_u32 s30, s2, 0x60000
	s_addc_u32 s31, s3, 0
	s_mov_b64 s[32:33], s[18:19]
	s_add_u32 s34, s18, 0x20000
	s_addc_u32 s35, s19, 0
	s_add_u32 s36, s18, 0x40000
	s_addc_u32 s37, s19, 0
	global_load_lds_dwordx4 v2, s[2:3]
	v_lshl_add_u64 v[8:9], v[4:5], 0, s[4:5]
	s_mov_b32 m0, s6
	s_mov_b64 s[6:7], 0x40000
	v_readfirstlane_b32 s8, v1
	global_load_lds_dwordx4 v[8:9], off
	v_lshl_add_u64 v[8:9], v[4:5], 0, s[6:7]
	s_mov_b32 m0, s8
	s_mov_b64 s[8:9], 0x60000
	v_or_b32_e32 v1, 0x6000, v139
	global_load_lds_dwordx4 v[8:9], off
	v_lshl_add_u64 v[8:9], v[4:5], 0, s[8:9]
	v_readfirstlane_b32 s8, v1
	v_or_b32_e32 v1, 0x8000, v139
	v_lshl_add_u64 v[6:7], s[18:19], 0, v[218:219]
	s_mov_b32 m0, s8
	v_readfirstlane_b32 s8, v1
	v_or_b32_e32 v1, 0xa000, v139
	global_load_lds_dwordx4 v[8:9], off
	s_mov_b32 m0, s8
	v_lshl_add_u64 v[8:9], v[6:7], 0, s[4:5]
	v_readfirstlane_b32 s4, v1
	v_or_b32_e32 v1, 0xc000, v139
	global_load_lds_dwordx4 v218, s[18:19]
	s_mov_b32 m0, s4
	v_readfirstlane_b32 s4, v1
	v_or_b32_e32 v1, 0xe000, v139
	global_load_lds_dwordx4 v[8:9], off
	v_lshl_add_u64 v[8:9], v[6:7], 0, s[6:7]
	s_mov_b32 m0, s4
	s_mov_b64 s[4:5], 0x80
	v_readfirstlane_b32 s6, v1
	v_or_b32_e32 v1, 0x10000, v139
	global_load_lds_dwordx4 v[8:9], off
	v_lshl_add_u64 v[8:9], v[4:5], 0, s[4:5]
	s_mov_b32 m0, s6
	s_mov_b64 s[6:7], 0x20080
	v_readfirstlane_b32 s8, v1
	v_or_b32_e32 v1, 0x12000, v139
	global_load_lds_dwordx4 v[8:9], off
	v_lshl_add_u64 v[8:9], v[4:5], 0, s[6:7]
	s_mov_b32 m0, s8
	v_readfirstlane_b32 s10, v1
	global_load_lds_dwordx4 v[8:9], off
	s_mov_b64 s[8:9], 0x40080
	s_mov_b32 m0, s10
	s_mov_b64 s[10:11], 0x60080
	v_or_b32_e32 v1, 0x14000, v139
	v_lshl_add_u64 v[8:9], v[4:5], 0, s[8:9]
	v_lshl_add_u64 v[4:5], v[4:5], 0, s[10:11]
	v_readfirstlane_b32 s10, v1
	global_load_lds_dwordx4 v[8:9], off
	s_mov_b32 m0, s10
	v_or_b32_e32 v1, 0x16000, v139
	global_load_lds_dwordx4 v[4:5], off
	v_lshl_add_u64 v[4:5], v[6:7], 0, s[4:5]
	v_readfirstlane_b32 s4, v1
	v_or_b32_e32 v1, 0x18000, v139
	s_mov_b32 m0, s4
	v_readfirstlane_b32 s4, v1
	v_or_b32_e32 v1, 0x1a000, v139
	global_load_lds_dwordx4 v[4:5], off
	v_lshl_add_u64 v[4:5], v[6:7], 0, s[6:7]
	s_mov_b32 m0, s4
	v_readfirstlane_b32 s4, v1
	global_load_lds_dwordx4 v[4:5], off
	v_lshl_add_u64 v[4:5], v[6:7], 0, s[8:9]
	s_mov_b32 m0, s4
	v_lshrrev_b32_e32 v2, 7, v0
	global_load_lds_dwordx4 v[4:5], off
	s_load_dwordx4 s[12:15], s[0:1], 0x38
	s_load_dwordx8 s[4:11], s[0:1], 0x18
	v_lshlrev_b32_e32 v4, 6, v0
	v_and_b32_e32 v138, 48, v0
	v_and_b32_e32 v4, 0x3c0, v4
	v_lshlrev_b32_e32 v6, 2, v0
	v_bfe_u32 v144, v0, 6, 1
	v_or_b32_e32 v14, v4, v138
	v_lshlrev_b32_e32 v5, 13, v2
	v_and_b32_e32 v15, 32, v6
	v_and_b32_e32 v1, 15, v0
	v_and_b32_e32 v216, 15, v0
	v_bfe_u32 v217, v0, 4, 2
	v_and_b32_e32 v6, 7, v216
	v_xor_b32_e32 v217, v217, v6
	v_lshlrev_b32_e32 v217, 4, v217
	v_lshl_or_b32 v216, v216, 7, v217
	v_bitop3_b32 v151, v4, v15, v138 bitop3:0x36
	v_or_b32_e32 v146, v5, v216
	v_xor_b32_e32 v214, 64, v146
	v_mul_u32_u24_e32 v152, 0x3000, v144
	v_lshl_or_b32 v145, v2, 6, s16
	v_or_b32_e32 v4, v145, v1
	v_ashrrev_i32_e32 v5, 31, v4
	s_waitcnt lgkmcnt(0)
	v_lshl_add_u64 v[4:5], v[4:5], 2, s[8:9]
	global_load_dword v150, v[4:5], off
	global_load_dword v149, v[4:5], off offset:64
	global_load_dword v148, v[4:5], off offset:128
	global_load_dword v147, v[4:5], off offset:192
	v_bitop3_b32 v153, v152, v14, v15 bitop3:0xf6
	v_mov_b32_e32 v48, v3
	v_mov_b32_e32 v49, v3
	v_mov_b32_e32 v50, v3
	v_mov_b32_e32 v51, v3
	v_mov_b32_e32 v52, v3
	v_mov_b32_e32 v53, v3
	v_mov_b32_e32 v54, v3
	v_mov_b32_e32 v55, v3
	v_mov_b32_e32 v56, v3
	v_mov_b32_e32 v57, v3
	v_mov_b32_e32 v58, v3
	v_mov_b32_e32 v59, v3
	v_mov_b32_e32 v60, v3
	v_mov_b32_e32 v61, v3
	v_mov_b32_e32 v62, v3
	v_mov_b32_e32 v63, v3
	v_mov_b32_e32 v64, v3
	v_mov_b32_e32 v65, v3
	v_mov_b32_e32 v66, v3
	v_mov_b32_e32 v67, v3
	v_mov_b32_e32 v68, v3
	v_mov_b32_e32 v69, v3
	v_mov_b32_e32 v70, v3
	v_mov_b32_e32 v71, v3
	v_mov_b32_e32 v72, v3
	v_mov_b32_e32 v73, v3
	v_mov_b32_e32 v74, v3
	v_mov_b32_e32 v75, v3
	v_mov_b32_e32 v76, v3
	v_mov_b32_e32 v77, v3
	v_mov_b32_e32 v86, v3
	v_mov_b32_e32 v87, v3
	v_mov_b32_e32 v88, v3
	v_mov_b32_e32 v89, v3
	v_mov_b32_e32 v98, v3
	v_mov_b32_e32 v99, v3
	v_mov_b32_e32 v100, v3
	v_mov_b32_e32 v101, v3
	v_mov_b32_e32 v130, v3
	v_mov_b32_e32 v131, v3
	v_mov_b32_e32 v132, v3
	v_mov_b32_e32 v133, v3
	v_mov_b32_e32 v78, v3
	v_mov_b32_e32 v79, v3
	v_mov_b32_e32 v80, v3
	v_mov_b32_e32 v81, v3
	v_mov_b32_e32 v82, v3
	v_mov_b32_e32 v83, v3
	v_mov_b32_e32 v84, v3
	v_mov_b32_e32 v85, v3
	v_mov_b32_e32 v90, v3
	v_mov_b32_e32 v91, v3
	v_mov_b32_e32 v92, v3
	v_mov_b32_e32 v93, v3
	v_mov_b32_e32 v94, v3
	v_mov_b32_e32 v95, v3
	v_mov_b32_e32 v96, v3
	v_mov_b32_e32 v97, v3
	v_mov_b32_e32 v102, v3
	v_mov_b32_e32 v103, v3
	v_mov_b32_e32 v104, v3
	v_mov_b32_e32 v105, v3
	v_mov_b32_e32 v106, v3
	v_mov_b32_e32 v107, v3
	v_mov_b32_e32 v108, v3
	v_mov_b32_e32 v109, v3
	v_mov_b32_e32 v110, v3
	v_mov_b32_e32 v111, v3
	v_mov_b32_e32 v112, v3
	v_mov_b32_e32 v113, v3
	v_mov_b32_e32 v114, v3
	v_mov_b32_e32 v115, v3
	v_mov_b32_e32 v116, v3
	v_mov_b32_e32 v117, v3
	v_mov_b32_e32 v118, v3
	v_mov_b32_e32 v119, v3
	v_mov_b32_e32 v120, v3
	v_mov_b32_e32 v121, v3
	v_mov_b32_e32 v122, v3
	v_mov_b32_e32 v123, v3
	v_mov_b32_e32 v124, v3
	v_mov_b32_e32 v125, v3
	v_mov_b32_e32 v134, v3
	v_mov_b32_e32 v135, v3
	v_mov_b32_e32 v136, v3
	v_mov_b32_e32 v137, v3
	v_mov_b32_e32 v126, v3
	v_mov_b32_e32 v127, v3
	v_mov_b32_e32 v128, v3
	v_mov_b32_e32 v129, v3
	s_waitcnt vmcnt(7) lgkmcnt(0)
	s_barrier
	ds_read_b128 v[42:45], v146
	ds_read_b128 v[38:41], v146 offset:2048
	ds_read_b128 v[10:13], v146 offset:4096
	ds_read_b128 v[6:9], v146 offset:6144
	ds_read_b128 v[22:25], v153 offset:32768
	ds_read_b128 v[18:21], v153 offset:34816
	ds_read_b128 v[30:33], v153 offset:36864
	ds_read_b128 v[26:29], v153 offset:38912
	ds_read_b128 v[34:37], v153 offset:40960
	ds_read_b128 v[14:17], v153 offset:43008
	v_lshl_or_b32 v2, v2, 15, v47
	v_lshl_or_b32 v2, v46, 11, v2
	v_lshl_add_u64 v[140:141], s[18:19], 0, v[2:3]
	v_lshl_add_u64 v[142:143], s[2:3], 0, v[2:3]
	s_mov_b32 s21, 0
	s_mov_b64 s[0:1], 0
	s_mov_b64 s[2:3], 0x100
	s_mov_b64 s[8:9], 0x20100
	s_mov_b64 s[16:17], 0x40100
	s_mov_b64 s[18:19], 0x60100
	v_mov_b32_e32 v2, v3
	v_mov_b32_e32 v4, v3
	v_mov_b32_e32 v5, v3
	v_mov_b32_e32 v46, v3
	v_mov_b32_e32 v47, v3
.LBB2_1:
	s_mul_i32 s22, s21, 0xe000
	v_add_u32_e32 v196, s22, v214
	v_add_u32_e32 v197, s22, v153
	s_add_u32 s46, s22, s45
	s_add_i32 s21, s21, 1
	s_waitcnt lgkmcnt(0)
	v_mfma_f32_16x16x32_f16 v[130:133], v[22:25], v[42:45], v[130:133]
	ds_read_b128 v[154:157], v196
	ds_read_b128 v[158:161], v196 offset:2048
	v_mfma_f32_16x16x32_f16 v[98:101], v[18:21], v[42:45], v[98:101]
	ds_read_b128 v[162:165], v196 offset:4096
	ds_read_b128 v[166:169], v196 offset:6144
	v_mfma_f32_16x16x32_f16 v[86:89], v[30:33], v[42:45], v[86:89]
	ds_read_b128 v[170:173], v197 offset:33792
	ds_read_b128 v[174:177], v197 offset:35840
	v_mfma_f32_16x16x32_f16 v[74:77], v[26:29], v[42:45], v[74:77]
	ds_read_b128 v[178:181], v197 offset:37888
	ds_read_b128 v[182:185], v197 offset:39936
	v_mfma_f32_16x16x32_f16 v[70:73], v[42:45], v[34:37], v[70:73]
	ds_read_b128 v[186:189], v197 offset:41984
	ds_read_b128 v[190:193], v197 offset:44032
	v_mfma_f32_16x16x32_f16 v[66:69], v[42:45], v[14:17], v[66:69]
	v_mfma_f32_16x16x32_f16 v[62:65], v[22:25], v[38:41], v[62:65]
	v_mfma_f32_16x16x32_f16 v[58:61], v[18:21], v[38:41], v[58:61]
	v_mfma_f32_16x16x32_f16 v[54:57], v[30:33], v[38:41], v[54:57]
	v_mfma_f32_16x16x32_f16 v[50:53], v[26:29], v[38:41], v[50:53]
	v_mfma_f32_16x16x32_f16 v[46:49], v[38:41], v[34:37], v[46:49]
	v_mfma_f32_16x16x32_f16 v[2:5], v[38:41], v[14:17], v[2:5]
	v_mfma_f32_16x16x32_f16 v[78:81], v[22:25], v[10:13], v[78:81]
	v_mfma_f32_16x16x32_f16 v[82:85], v[18:21], v[10:13], v[82:85]
	v_mfma_f32_16x16x32_f16 v[90:93], v[30:33], v[10:13], v[90:93]
	v_mfma_f32_16x16x32_f16 v[94:97], v[26:29], v[10:13], v[94:97]
	v_mfma_f32_16x16x32_f16 v[102:105], v[10:13], v[34:37], v[102:105]
	v_mfma_f32_16x16x32_f16 v[106:109], v[10:13], v[14:17], v[106:109]
	v_mfma_f32_16x16x32_f16 v[110:113], v[22:25], v[6:9], v[110:113]
	v_mfma_f32_16x16x32_f16 v[114:117], v[18:21], v[6:9], v[114:117]
	v_mfma_f32_16x16x32_f16 v[118:121], v[30:33], v[6:9], v[118:121]
	v_mfma_f32_16x16x32_f16 v[122:125], v[26:29], v[6:9], v[122:125]
	v_mfma_f32_16x16x32_f16 v[134:137], v[6:9], v[34:37], v[134:137]
	v_mfma_f32_16x16x32_f16 v[126:129], v[6:9], v[14:17], v[126:129]
	s_cmp_lg_u32 s21, 2
	s_cselect_b32 s21, s21, 0
	s_mul_i32 s22, s21, 0xe000
	v_add_u32_e32 v196, s22, v146
	v_add_u32_e32 v197, s22, v153
	s_waitcnt vmcnt(0) lgkmcnt(0)
	s_barrier
	s_mov_b32 m0, s46
	s_nop 0
	global_load_lds_dwordx4 v194, s[24:25]
	s_add_u32 m0, s46, 0x2000
	s_nop 0
	global_load_lds_dwordx4 v194, s[26:27]
	s_add_u32 m0, s46, 0x4000
	s_nop 0
	global_load_lds_dwordx4 v194, s[28:29]
	s_add_u32 m0, s46, 0x6000
	s_nop 0
	global_load_lds_dwordx4 v194, s[30:31]
	s_add_u32 m0, s46, 0x8000
	s_nop 0
	global_load_lds_dwordx4 v195, s[32:33]
	s_add_u32 m0, s46, 0xa000
	s_nop 0
	global_load_lds_dwordx4 v195, s[34:35]
	s_add_u32 m0, s46, 0xc000
	s_nop 0
	global_load_lds_dwordx4 v195, s[36:37]
	v_add_u32_e32 v194, 0x80, v194
	v_add_u32_e32 v195, 0x80, v195
	v_mfma_f32_16x16x32_f16 v[130:133], v[170:173], v[154:157], v[130:133]
	ds_read_b128 v[42:45], v196
	ds_read_b128 v[38:41], v196 offset:2048
	v_mfma_f32_16x16x32_f16 v[98:101], v[174:177], v[154:157], v[98:101]
	ds_read_b128 v[10:13], v196 offset:4096
	ds_read_b128 v[6:9], v196 offset:6144
	v_mfma_f32_16x16x32_f16 v[86:89], v[178:181], v[154:157], v[86:89]
	ds_read_b128 v[22:25], v197 offset:32768
	ds_read_b128 v[18:21], v197 offset:34816
	v_mfma_f32_16x16x32_f16 v[74:77], v[182:185], v[154:157], v[74:77]
	ds_read_b128 v[30:33], v197 offset:36864
	ds_read_b128 v[26:29], v197 offset:38912
	v_mfma_f32_16x16x32_f16 v[70:73], v[154:157], v[186:189], v[70:73]
	ds_read_b128 v[34:37], v197 offset:40960
	ds_read_b128 v[14:17], v197 offset:43008
	v_mfma_f32_16x16x32_f16 v[66:69], v[154:157], v[190:193], v[66:69]
	v_mfma_f32_16x16x32_f16 v[62:65], v[170:173], v[158:161], v[62:65]
	v_mfma_f32_16x16x32_f16 v[58:61], v[174:177], v[158:161], v[58:61]
	v_mfma_f32_16x16x32_f16 v[54:57], v[178:181], v[158:161], v[54:57]
	v_mfma_f32_16x16x32_f16 v[50:53], v[182:185], v[158:161], v[50:53]
	v_mfma_f32_16x16x32_f16 v[46:49], v[158:161], v[186:189], v[46:49]
	v_mfma_f32_16x16x32_f16 v[2:5], v[158:161], v[190:193], v[2:5]
	v_mfma_f32_16x16x32_f16 v[78:81], v[170:173], v[162:165], v[78:81]
	v_mfma_f32_16x16x32_f16 v[82:85], v[174:177], v[162:165], v[82:85]
	v_mfma_f32_16x16x32_f16 v[90:93], v[178:181], v[162:165], v[90:93]
	v_mfma_f32_16x16x32_f16 v[94:97], v[182:185], v[162:165], v[94:97]
	v_mfma_f32_16x16x32_f16 v[102:105], v[162:165], v[186:189], v[102:105]
	v_mfma_f32_16x16x32_f16 v[106:109], v[162:165], v[190:193], v[106:109]
	v_mfma_f32_16x16x32_f16 v[110:113], v[170:173], v[166:169], v[110:113]
	v_mfma_f32_16x16x32_f16 v[114:117], v[174:177], v[166:169], v[114:117]
	v_mfma_f32_16x16x32_f16 v[118:121], v[178:181], v[166:169], v[118:121]
	v_mfma_f32_16x16x32_f16 v[122:125], v[182:185], v[166:169], v[122:125]
	v_mfma_f32_16x16x32_f16 v[134:137], v[166:169], v[186:189], v[134:137]
	v_mfma_f32_16x16x32_f16 v[126:129], v[166:169], v[190:193], v[126:129]
	s_add_u32 s0, s0, 0x80
	s_addc_u32 s1, s1, 0
	s_cmpk_eq_i32 s0, 0x700
	s_cbranch_scc0 .LBB2_1
	s_waitcnt lgkmcnt(0)
	v_mfma_f32_16x16x32_f16 v[130:133], v[22:25], v[42:45], v[130:133]
	ds_read_b128 v[140:143], v214
	ds_read_b128 v[154:157], v214 offset:2048
	v_mfma_f32_16x16x32_f16 v[98:101], v[18:21], v[42:45], v[98:101]
	ds_read_b128 v[158:161], v214 offset:4096
	ds_read_b128 v[162:165], v214 offset:6144
	v_mfma_f32_16x16x32_f16 v[86:89], v[30:33], v[42:45], v[86:89]
	ds_read_b128 v[166:169], v153 offset:33792
	ds_read_b128 v[170:173], v153 offset:35840
	v_mfma_f32_16x16x32_f16 v[74:77], v[26:29], v[42:45], v[74:77]
	ds_read_b128 v[174:177], v153 offset:37888
	ds_read_b128 v[178:181], v153 offset:39936
	v_mfma_f32_16x16x32_f16 v[70:73], v[42:45], v[34:37], v[70:73]
	ds_read_b128 v[182:185], v153 offset:41984
	ds_read_b128 v[186:189], v153 offset:44032
	v_mfma_f32_16x16x32_f16 v[42:45], v[42:45], v[14:17], v[66:69]
	v_mfma_f32_16x16x32_f16 v[62:65], v[22:25], v[38:41], v[62:65]
	v_mfma_f32_16x16x32_f16 v[58:61], v[18:21], v[38:41], v[58:61]
	v_mfma_f32_16x16x32_f16 v[54:57], v[30:33], v[38:41], v[54:57]
	v_mfma_f32_16x16x32_f16 v[50:53], v[26:29], v[38:41], v[50:53]
	v_mfma_f32_16x16x32_f16 v[46:49], v[38:41], v[34:37], v[46:49]
	v_mfma_f32_16x16x32_f16 v[2:5], v[38:41], v[14:17], v[2:5]
	v_mfma_f32_16x16x32_f16 v[38:41], v[22:25], v[10:13], v[78:81]
	v_mfma_f32_16x16x32_f16 v[66:69], v[18:21], v[10:13], v[82:85]
	v_mfma_f32_16x16x32_f16 v[78:81], v[30:33], v[10:13], v[90:93]
	v_mfma_f32_16x16x32_f16 v[82:85], v[26:29], v[10:13], v[94:97]
	v_mfma_f32_16x16x32_f16 v[90:93], v[10:13], v[34:37], v[102:105]
	v_mfma_f32_16x16x32_f16 v[94:97], v[10:13], v[14:17], v[106:109]
	v_mfma_f32_16x16x32_f16 v[22:25], v[22:25], v[6:9], v[110:113]
	v_mfma_f32_16x16x32_f16 v[102:105], v[18:21], v[6:9], v[114:117]
	v_or_b32_e32 v21, v151, v152
	v_and_b32_e32 v20, 63, v0
	v_mfma_f32_16x16x32_f16 v[30:33], v[30:33], v[6:9], v[118:121]
	v_mfma_f32_16x16x32_f16 v[26:29], v[26:29], v[6:9], v[122:125]
	v_mfma_f32_16x16x32_f16 v[34:37], v[6:9], v[34:37], v[134:137]
	v_mfma_f32_16x16x32_f16 v[6:9], v[6:9], v[14:17], v[126:129]
	v_add_u32_e32 v10, 0x16800, v21
	s_waitcnt vmcnt(0) lgkmcnt(0)
	s_waitcnt lgkmcnt(0)
	v_mfma_f32_16x16x32_f16 v[16:19], v[166:169], v[140:143], v[130:133]
	s_barrier
	ds_read_b128 v[106:109], v146 offset:57344
	ds_read_b128 v[110:113], v146 offset:59392
	v_mfma_f32_16x16x32_f16 v[98:101], v[170:173], v[140:143], v[98:101]
	ds_read_b128 v[114:117], v146 offset:61440
	ds_read_b128 v[12:15], v146 offset:63488
	v_add_u32_e32 v0, 0x16000, v21
	v_mfma_f32_16x16x32_f16 v[86:89], v[174:177], v[140:143], v[86:89]
	ds_read_b128 v[122:125], v10
	v_add_u32_e32 v10, 0x17000, v21
	ds_read_b128 v[118:121], v0
	v_mfma_f32_16x16x32_f16 v[74:77], v[178:181], v[140:143], v[74:77]
	ds_read_b128 v[126:129], v10
	v_add_u32_e32 v10, 0x17800, v21
	ds_read_b128 v[130:133], v10
	v_mfma_f32_16x16x32_f16 v[70:73], v[140:143], v[182:185], v[70:73]
	ds_read_b128 v[134:137], v0 offset:8192
	ds_read_b128 v[190:193], v0 offset:10240
	v_mfma_f32_16x16x32_f16 v[42:45], v[140:143], v[186:189], v[42:45]
	v_mfma_f32_16x16x32_f16 v[62:65], v[166:169], v[154:157], v[62:65]
	v_mfma_f32_16x16x32_f16 v[58:61], v[170:173], v[154:157], v[58:61]
	v_mfma_f32_16x16x32_f16 v[54:57], v[174:177], v[154:157], v[54:57]
	v_mfma_f32_16x16x32_f16 v[50:53], v[178:181], v[154:157], v[50:53]
	v_mfma_f32_16x16x32_f16 v[46:49], v[154:157], v[182:185], v[46:49]
	v_mfma_f32_16x16x32_f16 v[140:143], v[154:157], v[186:189], v[2:5]
	v_mfma_f32_16x16x32_f16 v[38:41], v[166:169], v[158:161], v[38:41]
	v_mfma_f32_16x16x32_f16 v[66:69], v[170:173], v[158:161], v[66:69]
	v_mfma_f32_16x16x32_f16 v[78:81], v[174:177], v[158:161], v[78:81]
	v_mfma_f32_16x16x32_f16 v[82:85], v[178:181], v[158:161], v[82:85]
	v_mfma_f32_16x16x32_f16 v[90:93], v[158:161], v[182:185], v[90:93]
	v_mfma_f32_16x16x32_f16 v[94:97], v[158:161], v[186:189], v[94:97]
	v_mfma_f32_16x16x32_f16 v[22:25], v[166:169], v[162:165], v[22:25]
	v_mfma_f32_16x16x32_f16 v[102:105], v[170:173], v[162:165], v[102:105]
	v_mfma_f32_16x16x32_f16 v[30:33], v[174:177], v[162:165], v[30:33]
	v_mfma_f32_16x16x32_f16 v[26:29], v[178:181], v[162:165], v[26:29]
	v_mfma_f32_16x16x32_f16 v[34:37], v[162:165], v[182:185], v[34:37]
	v_mfma_f32_16x16x32_f16 v[152:155], v[162:165], v[186:189], v[6:9]
	s_waitcnt lgkmcnt(0)
	v_mfma_f32_16x16x32_f16 v[156:159], v[118:121], v[106:109], v[16:19]
	s_movk_i32 s0, 0x7c0
	ds_read_b128 v[202:205], v0 offset:9216
	ds_read_b128 v[206:209], v0 offset:11264
	v_lshlrev_b32_e32 v16, 6, v144
	v_mov_b32_e32 v17, 0
	v_mov_b32_e32 v139, v17
	v_lshl_add_u64 v[4:5], s[6:7], 0, v[16:17]
	v_lshl_add_u64 v[8:9], v[4:5], 0, v[138:139]
	s_waitcnt vmcnt(0)
	v_lshlrev_b32_e32 v4, 5, v150
	v_lshl_add_u64 v[2:3], s[4:5], 0, v[16:17]
	v_ashrrev_i32_e32 v5, 31, v4
	v_lshl_add_u64 v[2:3], v[2:3], 0, v[138:139]
	v_lshlrev_b64 v[4:5], 2, v[4:5]
	v_lshl_add_u64 v[6:7], v[2:3], 0, v[4:5]
	v_lshl_add_u64 v[4:5], v[8:9], 0, v[4:5]
	v_mfma_f32_16x16x32_f16 v[98:101], v[122:125], v[106:109], v[98:101]
	global_load_dwordx4 v[160:163], v[6:7], off
	v_lshlrev_b32_e32 v18, 5, v147
	v_ashrrev_i32_e32 v19, 31, v18
	v_mfma_f32_16x16x32_f16 v[86:89], v[126:129], v[106:109], v[86:89]
	v_lshlrev_b64 v[18:19], 2, v[18:19]
	ds_read_b128 v[172:175], v214 offset:61440
	ds_read_b128 v[176:179], v214 offset:63488
	v_mfma_f32_16x16x32_f16 v[74:77], v[130:133], v[106:109], v[74:77]
	v_mfma_f32_16x16x32_f16 v[70:73], v[106:109], v[134:137], v[70:73]
	v_mfma_f32_16x16x32_f16 v[42:45], v[106:109], v[190:193], v[42:45]
	global_load_dwordx4 v[106:109], v[4:5], off
	v_lshlrev_b32_e32 v4, 5, v149
	v_ashrrev_i32_e32 v5, 31, v4
	v_lshlrev_b64 v[4:5], 2, v[4:5]
	v_lshl_add_u64 v[6:7], v[2:3], 0, v[4:5]
	v_lshl_add_u64 v[4:5], v[8:9], 0, v[4:5]
	global_load_dwordx4 v[168:171], v[4:5], off
	global_load_dwordx4 v[164:167], v[6:7], off
	v_lshlrev_b32_e32 v4, 5, v148
	v_ashrrev_i32_e32 v5, 31, v4
	v_lshlrev_b64 v[10:11], 2, v[4:5]
	v_lshl_add_u64 v[4:5], v[2:3], 0, v[10:11]
	v_lshl_add_u64 v[10:11], v[8:9], 0, v[10:11]
	global_load_dwordx4 v[210:213], v[10:11], off
	v_lshl_add_u64 v[2:3], v[2:3], 0, v[18:19]
	global_load_dwordx4 v[4:7], v[4:5], off
	v_lshl_add_u64 v[8:9], v[8:9], 0, v[18:19]
	v_add_u32_e32 v18, 0x16400, v21
	v_ashrrev_i32_e32 v10, 7, v145
	ds_read_b128 v[180:183], v18
	v_add_u32_e32 v18, 0x17400, v21
	v_and_b32_e32 v10, -16, v10
	v_add_u32_e32 v19, 0x16c00, v21
	ds_read_b128 v[194:197], v18
	v_add_u32_e32 v18, s20, v10
	global_load_dwordx4 v[8:11], v[8:9], off
	ds_read_b128 v[184:187], v19
	v_add_u32_e32 v19, 0x17c00, v21
	v_and_or_b32 v21, v145, s0, v1
	global_load_dwordx4 v[0:3], v[2:3], off
	v_mfma_f32_16x16x32_f16 v[62:65], v[118:121], v[110:113], v[62:65]
	ds_read_b128 v[198:201], v19
	v_ashrrev_i32_e32 v19, 31, v18
	ds_read_b128 v[148:151], v214 offset:59392
	v_mfma_f32_16x16x32_f16 v[58:61], v[122:125], v[110:113], v[58:61]
	v_mfma_f32_16x16x32_f16 v[54:57], v[126:129], v[110:113], v[54:57]
	v_mfma_f32_16x16x32_f16 v[50:53], v[130:133], v[110:113], v[50:53]
	v_mfma_f32_16x16x32_f16 v[46:49], v[110:113], v[134:137], v[46:49]
	v_mfma_f32_16x16x32_f16 v[110:113], v[110:113], v[190:193], v[140:143]
	s_nop 2
	ds_read_b128 v[140:143], v214 offset:57344
	v_mfma_f32_16x16x32_f16 v[38:41], v[118:121], v[114:117], v[38:41]
	v_mfma_f32_16x16x32_f16 v[66:69], v[122:125], v[114:117], v[66:69]
	v_mfma_f32_16x16x32_f16 v[78:81], v[126:129], v[114:117], v[78:81]
	v_mfma_f32_16x16x32_f16 v[82:85], v[130:133], v[114:117], v[82:85]
	v_mfma_f32_16x16x32_f16 v[90:93], v[114:117], v[134:137], v[90:93]
	v_mfma_f32_16x16x32_f16 v[94:97], v[114:117], v[190:193], v[94:97]
	s_waitcnt lgkmcnt(0)
	v_mfma_f32_16x16x32_f16 v[114:117], v[180:183], v[140:143], v[156:159]
	v_mfma_f32_16x16x32_f16 v[98:101], v[184:187], v[140:143], v[98:101]
	v_mfma_f32_16x16x32_f16 v[22:25], v[118:121], v[12:15], v[22:25]
	s_waitcnt vmcnt(6)
	s_nop 4
	v_pk_mul_f32 v[120:121], v[114:115], v[106:107] op_sel_hi:[1,0]
	v_lshlrev_b64 v[118:119], 17, v[18:19]
	v_lshl_or_b32 v118, v21, 6, v118
	v_mfma_f32_16x16x32_f16 v[102:105], v[122:125], v[12:15], v[102:105]
	v_mul_f32_e64 v122, v116, v107
	v_mul_f32_e64 v123, v117, v107
	v_pk_fma_f32 v[124:125], v[114:115], v[160:161], v[120:121] op_sel:[0,0,1] op_sel_hi:[1,1,0] neg_lo:[0,0,1] neg_hi:[0,0,1]
	v_pk_fma_f32 v[114:115], v[114:115], v[160:161], v[120:121] op_sel:[0,0,1] op_sel_hi:[1,0,0]
	v_pk_fma_f32 v[120:121], v[116:117], v[160:161], v[122:123] op_sel:[0,1,1] op_sel_hi:[1,1,0] neg_lo:[0,0,1] neg_hi:[0,0,1]
	v_pk_fma_f32 v[116:117], v[116:117], v[160:161], v[122:123] op_sel:[0,1,1] op_sel_hi:[1,1,0]
	v_cvt_pk_f16_f32 v114, v124, v115
	v_cvt_pk_f16_f32 v115, v120, v117
	v_pk_mul_f32 v[116:117], v[98:99], v[108:109] op_sel_hi:[1,0]
	v_mov_b32_e32 v122, v163
	v_pk_fma_f32 v[120:121], v[98:99], v[162:163], v[116:117] op_sel:[0,0,1] op_sel_hi:[1,1,0] neg_lo:[0,0,1] neg_hi:[0,0,1]
	v_pk_fma_f32 v[98:99], v[98:99], v[162:163], v[116:117] op_sel:[0,0,1] op_sel_hi:[1,0,0]
	v_mfma_f32_16x16x32_f16 v[30:33], v[126:129], v[12:15], v[30:33]
	v_cvt_pk_f16_f32 v116, v120, v99
	v_mov_b32_e32 v120, v109
	v_pk_mul_f32 v[98:99], v[100:101], v[120:121] op_sel_hi:[1,0]
	v_mfma_f32_16x16x32_f16 v[26:29], v[130:133], v[12:15], v[26:29]
	v_fma_f32 v124, v100, v122, -v99
	v_fma_f32 v125, v101, v122, -v98
	v_pk_fma_f32 v[98:99], v[100:101], v[122:123], v[98:99] op_sel:[0,0,1] op_sel_hi:[1,0,0]
	s_nop 0
	v_cvt_pk_f16_f32 v117, v124, v99
	v_lshlrev_b64 v[124:125], 1, v[118:119]
	v_lshl_add_u64 v[126:127], s[10:11], 0, v[124:125]
	v_mfma_f32_16x16x32_f16 v[34:37], v[12:15], v[134:137], v[34:37]
	v_mfma_f32_16x16x32_f16 v[98:101], v[12:15], v[190:193], v[152:155]
	v_lshl_add_u64 v[12:13], v[126:127], 0, v[16:17]
	v_lshl_add_u64 v[126:127], v[12:13], 0, v[138:139]
	global_store_dwordx4 v[126:127], v[114:117], off sc1
	v_mfma_f32_16x16x32_f16 v[12:15], v[194:197], v[140:143], v[86:89]
	v_mfma_f32_16x16x32_f16 v[74:77], v[198:201], v[140:143], v[74:77]
	v_mfma_f32_16x16x32_f16 v[58:61], v[184:187], v[148:151], v[58:61]
	s_nop 5
	v_mul_f32_e64 v86, v12, v106
	v_mul_f32_e64 v87, v13, v106
	v_pk_fma_f32 v[88:89], v[12:13], v[160:161], v[86:87] op_sel:[0,0,1] op_sel_hi:[1,1,0] neg_lo:[0,0,1] neg_hi:[0,0,1]
	v_pk_fma_f32 v[12:13], v[12:13], v[160:161], v[86:87] op_sel:[0,0,1] op_sel_hi:[1,0,0]
	v_mfma_f32_16x16x32_f16 v[54:57], v[194:197], v[148:151], v[54:57]
	v_cvt_pk_f16_f32 v86, v88, v13
	v_pk_mul_f32 v[12:13], v[14:15], v[106:107] op_sel:[0,1]
	s_nop 0
	v_pk_fma_f32 v[88:89], v[14:15], v[160:161], v[12:13] op_sel:[0,1,1] op_sel_hi:[1,1,0] neg_lo:[0,0,1] neg_hi:[0,0,1]
	v_pk_fma_f32 v[12:13], v[14:15], v[160:161], v[12:13] op_sel:[0,1,1] op_sel_hi:[1,1,0]
	v_mfma_f32_16x16x32_f16 v[50:53], v[198:201], v[148:151], v[50:53]
	v_cvt_pk_f16_f32 v87, v88, v13
	v_pk_mul_f32 v[88:89], v[74:75], v[108:109] op_sel_hi:[1,0]
	v_mfma_f32_16x16x32_f16 v[12:15], v[140:143], v[206:209], v[42:45]
	s_nop 2
	v_fma_f32 v42, v74, v162, -v89
	v_fma_f32 v43, v75, v163, -v88
	v_pk_fma_f32 v[44:45], v[74:75], v[162:163], v[88:89] op_sel:[0,0,1] op_sel_hi:[1,0,0]
	v_mfma_f32_16x16x32_f16 v[38:41], v[180:183], v[172:175], v[38:41]
	v_cvt_pk_f16_f32 v88, v42, v45
	v_mfma_f32_16x16x32_f16 v[42:45], v[180:183], v[148:151], v[62:65]
	s_nop 2
	v_mul_f32_e64 v62, v76, v120
	v_mul_f32_e64 v63, v77, v120
	v_mfma_f32_16x16x32_f16 v[66:69], v[184:187], v[172:175], v[66:69]
	v_fma_f32 v64, v76, v122, -v63
	v_fma_f32 v65, v77, v122, -v62
	v_pk_fma_f32 v[62:63], v[76:77], v[122:123], v[62:63] op_sel:[0,0,1] op_sel_hi:[1,0,0]
	s_nop 0
	v_cvt_pk_f16_f32 v89, v64, v63
	v_lshl_add_u64 v[62:63], s[12:13], 0, v[124:125]
	v_lshl_add_u64 v[62:63], v[62:63], 0, v[16:17]
	v_lshl_add_u64 v[106:107], v[62:63], 0, v[138:139]
	s_waitcnt vmcnt(6)
	v_pk_mul_f32 v[62:63], v[42:43], v[168:169] op_sel_hi:[1,0]
	global_store_dwordx4 v[106:107], v[86:89], off sc1
	s_waitcnt vmcnt(6)
	v_pk_fma_f32 v[64:65], v[42:43], v[164:165], v[62:63] op_sel:[0,0,1] op_sel_hi:[1,1,0] neg_lo:[0,0,1] neg_hi:[0,0,1]
	v_pk_fma_f32 v[42:43], v[42:43], v[164:165], v[62:63] op_sel:[0,0,1] op_sel_hi:[1,0,0]
	v_pk_mul_f32 v[62:63], v[44:45], v[168:169] op_sel:[0,1]
	v_cvt_pk_f16_f32 v42, v64, v43
	v_pk_fma_f32 v[74:75], v[44:45], v[164:165], v[62:63] op_sel:[0,1,1] op_sel_hi:[1,1,0] neg_lo:[0,0,1] neg_hi:[0,0,1]
	v_pk_fma_f32 v[44:45], v[44:45], v[164:165], v[62:63] op_sel:[0,1,1] op_sel_hi:[1,1,0]
	v_mov_b32_e32 v86, v171
	v_cvt_pk_f16_f32 v43, v74, v45
	v_pk_mul_f32 v[44:45], v[58:59], v[170:171] op_sel_hi:[1,0]
	v_mov_b32_e32 v88, v167
	v_pk_fma_f32 v[74:75], v[58:59], v[166:167], v[44:45] op_sel:[0,0,1] op_sel_hi:[1,1,0] neg_lo:[0,0,1] neg_hi:[0,0,1]
	v_pk_fma_f32 v[44:45], v[58:59], v[166:167], v[44:45] op_sel:[0,0,1] op_sel_hi:[1,0,0]
	v_pk_mul_f32 v[58:59], v[60:61], v[86:87] op_sel_hi:[1,0]
	v_cvt_pk_f16_f32 v44, v74, v45
	v_pk_fma_f32 v[108:109], v[60:61], v[88:89], v[58:59] op_sel:[0,0,1] op_sel_hi:[1,0,0] neg_lo:[0,0,1] neg_hi:[0,0,1]
	v_pk_fma_f32 v[58:59], v[60:61], v[88:89], v[58:59] op_sel:[0,0,1] op_sel_hi:[1,0,0]
	v_mfma_f32_16x16x32_f16 v[74:77], v[194:197], v[172:175], v[78:81]
	v_cvt_pk_f16_f32 v45, v108, v59
	global_store_dwordx4 v[126:127], v[42:45], off offset:2048 sc1
	v_pk_mul_f32 v[58:59], v[54:55], v[168:169] op_sel_hi:[1,0]
	v_mfma_f32_16x16x32_f16 v[22:25], v[180:183], v[176:179], v[22:25]
	v_fma_f32 v78, v54, v164, -v59
	v_fma_f32 v79, v55, v165, -v58
	v_pk_fma_f32 v[54:55], v[54:55], v[164:165], v[58:59] op_sel:[0,0,1] op_sel_hi:[1,0,0]
	v_mfma_f32_16x16x32_f16 v[42:45], v[198:201], v[172:175], v[82:85]
	v_cvt_pk_f16_f32 v54, v78, v55
	s_nop 1
	v_pk_mul_f32 v[82:83], v[56:57], v[168:169] op_sel:[0,1]
	v_mfma_f32_16x16x32_f16 v[30:33], v[194:197], v[176:179], v[30:33]
	v_fma_f32 v84, v56, v165, -v83
	v_fma_f32 v85, v57, v165, -v82
	v_pk_fma_f32 v[56:57], v[56:57], v[164:165], v[82:83] op_sel:[0,1,1] op_sel_hi:[1,1,0]
	s_nop 0
	v_cvt_pk_f16_f32 v55, v84, v57
	v_pk_mul_f32 v[56:57], v[50:51], v[170:171] op_sel_hi:[1,0]
	v_mfma_f32_16x16x32_f16 v[26:29], v[198:201], v[176:179], v[26:29]
	v_fma_f32 v82, v50, v166, -v57
	v_fma_f32 v83, v51, v167, -v56
	v_pk_fma_f32 v[50:51], v[50:51], v[166:167], v[56:57] op_sel:[0,0,1] op_sel_hi:[1,0,0]
	s_nop 0
	v_cvt_pk_f16_f32 v56, v82, v51
	v_pk_mul_f32 v[50:51], v[52:53], v[86:87] op_sel_hi:[1,0]
	v_mfma_f32_16x16x32_f16 v[82:85], v[184:187], v[176:179], v[102:105]
	v_fma_f32 v86, v52, v88, -v51
	v_fma_f32 v87, v53, v88, -v50
	v_pk_fma_f32 v[50:51], v[52:53], v[88:89], v[50:51] op_sel:[0,0,1] op_sel_hi:[1,0,0]
	s_nop 0
	v_cvt_pk_f16_f32 v57, v86, v51
	global_store_dwordx4 v[106:107], v[54:57], off offset:2048 sc1
	s_waitcnt vmcnt(7)
	v_pk_mul_f32 v[50:51], v[38:39], v[210:211] op_sel_hi:[1,0]
	v_mfma_f32_16x16x32_f16 v[70:73], v[140:143], v[202:205], v[70:73]
	v_mul_f32_e64 v56, v40, v211
	v_mul_f32_e64 v57, v41, v211
	s_waitcnt vmcnt(6)
	v_pk_fma_f32 v[52:53], v[38:39], v[4:5], v[50:51] op_sel:[0,0,1] op_sel_hi:[1,1,0] neg_lo:[0,0,1] neg_hi:[0,0,1]
	v_pk_fma_f32 v[38:39], v[38:39], v[4:5], v[50:51] op_sel:[0,0,1] op_sel_hi:[1,0,0]
	v_pk_fma_f32 v[86:87], v[40:41], v[4:5], v[56:57] op_sel:[0,1,1] op_sel_hi:[1,1,0] neg_lo:[0,0,1] neg_hi:[0,0,1]
	v_pk_fma_f32 v[40:41], v[40:41], v[4:5], v[56:57] op_sel:[0,1,1] op_sel_hi:[1,1,0]
	v_cvt_pk_f16_f32 v38, v52, v39
	v_cvt_pk_f16_f32 v39, v86, v41
	v_pk_mul_f32 v[40:41], v[66:67], v[212:213] op_sel_hi:[1,0]
	v_or_b32_e32 v54, 0x800, v118
	v_pk_fma_f32 v[56:57], v[66:67], v[6:7], v[40:41] op_sel:[0,0,1] op_sel_hi:[1,1,0] neg_lo:[0,0,1] neg_hi:[0,0,1]
	v_pk_fma_f32 v[40:41], v[66:67], v[6:7], v[40:41] op_sel:[0,0,1] op_sel_hi:[1,0,0]
	v_mov_b32_e32 v55, v119
	v_cvt_pk_f16_f32 v40, v56, v41
	v_mov_b32_e32 v56, v213
	v_pk_mul_f32 v[66:67], v[68:69], v[56:57] op_sel_hi:[1,0]
	v_mov_b32_e32 v86, v7
	v_pk_fma_f32 v[88:89], v[68:69], v[86:87], v[66:67] op_sel:[0,0,1] op_sel_hi:[1,0,0] neg_lo:[0,0,1] neg_hi:[0,0,1]
	v_pk_fma_f32 v[66:67], v[68:69], v[86:87], v[66:67] op_sel:[0,0,1] op_sel_hi:[1,0,0]
	v_lshlrev_b64 v[54:55], 1, v[54:55]
	v_cvt_pk_f16_f32 v41, v88, v67
	v_lshl_add_u64 v[66:67], s[10:11], 0, v[54:55]
	v_lshl_add_u64 v[66:67], v[66:67], 0, v[16:17]
	v_lshl_add_u64 v[66:67], v[66:67], 0, v[138:139]
	global_store_dwordx4 v[66:67], v[38:41], off sc1
	v_or_b32_e32 v118, 0xc00, v118
	v_mfma_f32_16x16x32_f16 v[46:49], v[148:151], v[202:205], v[46:49]
	v_mul_f32_e64 v38, v74, v210
	v_mul_f32_e64 v39, v75, v210
	v_pk_fma_f32 v[40:41], v[74:75], v[4:5], v[38:39] op_sel:[0,0,1] op_sel_hi:[1,1,0] neg_lo:[0,0,1] neg_hi:[0,0,1]
	v_pk_fma_f32 v[38:39], v[74:75], v[4:5], v[38:39] op_sel:[0,0,1] op_sel_hi:[1,0,0]
	v_mfma_f32_16x16x32_f16 v[58:61], v[172:175], v[202:205], v[90:93]
	v_cvt_pk_f16_f32 v38, v40, v39
	v_pk_mul_f32 v[40:41], v[76:77], v[210:211] op_sel:[0,1]
	s_nop 0
	v_pk_fma_f32 v[66:67], v[76:77], v[4:5], v[40:41] op_sel:[0,1,1] op_sel_hi:[1,1,0] neg_lo:[0,0,1] neg_hi:[0,0,1]
	v_pk_fma_f32 v[4:5], v[76:77], v[4:5], v[40:41] op_sel:[0,1,1] op_sel_hi:[1,1,0]
	v_mfma_f32_16x16x32_f16 v[34:37], v[176:179], v[202:205], v[34:37]
	v_cvt_pk_f16_f32 v39, v66, v5
	v_pk_mul_f32 v[4:5], v[42:43], v[212:213] op_sel_hi:[1,0]
	s_nop 0
	v_pk_fma_f32 v[40:41], v[42:43], v[6:7], v[4:5] op_sel:[0,0,1] op_sel_hi:[1,1,0] neg_lo:[0,0,1] neg_hi:[0,0,1]
	v_pk_fma_f32 v[4:5], v[42:43], v[6:7], v[4:5] op_sel:[0,0,1] op_sel_hi:[1,0,0]
	v_mfma_f32_16x16x32_f16 v[62:65], v[148:151], v[206:209], v[110:113]
	v_cvt_pk_f16_f32 v40, v40, v5
	v_pk_mul_f32 v[4:5], v[44:45], v[56:57] op_sel_hi:[1,0]
	s_nop 0
	v_pk_fma_f32 v[6:7], v[44:45], v[86:87], v[4:5] op_sel:[0,0,1] op_sel_hi:[1,0,0] neg_lo:[0,0,1] neg_hi:[0,0,1]
	v_pk_fma_f32 v[4:5], v[44:45], v[86:87], v[4:5] op_sel:[0,0,1] op_sel_hi:[1,0,0]
	v_mfma_f32_16x16x32_f16 v[78:81], v[172:175], v[206:209], v[94:97]
	v_cvt_pk_f16_f32 v41, v6, v5
	v_lshl_add_u64 v[4:5], s[12:13], 0, v[54:55]
	v_lshl_add_u64 v[4:5], v[4:5], 0, v[16:17]
	v_lshl_add_u64 v[4:5], v[4:5], 0, v[138:139]
	global_store_dwordx4 v[4:5], v[38:41], off sc1
	s_waitcnt vmcnt(7)
	v_pk_mul_f32 v[4:5], v[22:23], v[8:9] op_sel_hi:[1,0]
	v_mfma_f32_16x16x32_f16 v[50:53], v[176:179], v[206:209], v[98:101]
	s_waitcnt vmcnt(6)
	v_pk_fma_f32 v[6:7], v[22:23], v[0:1], v[4:5] op_sel:[0,0,1] op_sel_hi:[1,1,0] neg_lo:[0,0,1] neg_hi:[0,0,1]
	v_pk_fma_f32 v[4:5], v[22:23], v[0:1], v[4:5] op_sel:[0,0,1] op_sel_hi:[1,0,0]
	v_mov_b32_e32 v38, v3
	v_cvt_pk_f16_f32 v4, v6, v5
	v_pk_mul_f32 v[6:7], v[24:25], v[8:9] op_sel:[0,1]
	s_nop 0
	v_pk_fma_f32 v[22:23], v[24:25], v[0:1], v[6:7] op_sel:[0,1,1] op_sel_hi:[1,1,0] neg_lo:[0,0,1] neg_hi:[0,0,1]
	v_pk_fma_f32 v[6:7], v[24:25], v[0:1], v[6:7] op_sel:[0,1,1] op_sel_hi:[1,1,0]
	s_nop 0
	v_cvt_pk_f16_f32 v5, v22, v7
	v_pk_mul_f32 v[6:7], v[82:83], v[10:11] op_sel_hi:[1,0]
	s_nop 0
	v_pk_fma_f32 v[22:23], v[82:83], v[2:3], v[6:7] op_sel:[0,0,1] op_sel_hi:[1,1,0] neg_lo:[0,0,1] neg_hi:[0,0,1]
	v_pk_fma_f32 v[6:7], v[82:83], v[2:3], v[6:7] op_sel:[0,0,1] op_sel_hi:[1,0,0]
	s_nop 0
	v_cvt_pk_f16_f32 v6, v22, v7
	v_mov_b32_e32 v22, v11
	v_pk_mul_f32 v[24:25], v[84:85], v[22:23] op_sel_hi:[1,0]
	s_nop 0
	v_pk_fma_f32 v[40:41], v[84:85], v[38:39], v[24:25] op_sel:[0,0,1] op_sel_hi:[1,0,0] neg_lo:[0,0,1] neg_hi:[0,0,1]
	v_pk_fma_f32 v[24:25], v[84:85], v[38:39], v[24:25] op_sel:[0,0,1] op_sel_hi:[1,0,0]
	s_nop 0
	v_cvt_pk_f16_f32 v7, v40, v25
	v_lshlrev_b64 v[24:25], 1, v[118:119]
	v_lshl_add_u64 v[40:41], s[10:11], 0, v[24:25]
	v_lshl_add_u64 v[40:41], v[40:41], 0, v[16:17]
	v_lshl_add_u64 v[40:41], v[40:41], 0, v[138:139]
	global_store_dwordx4 v[40:41], v[4:7], off sc1
	s_nop 1
	v_pk_mul_f32 v[4:5], v[30:31], v[8:9] op_sel_hi:[1,0]
	s_nop 0
	v_pk_fma_f32 v[6:7], v[30:31], v[0:1], v[4:5] op_sel:[0,0,1] op_sel_hi:[1,1,0] neg_lo:[0,0,1] neg_hi:[0,0,1]
	v_pk_fma_f32 v[4:5], v[30:31], v[0:1], v[4:5] op_sel:[0,0,1] op_sel_hi:[1,0,0]
	s_nop 0
	v_cvt_pk_f16_f32 v4, v6, v5
	v_pk_mul_f32 v[6:7], v[32:33], v[8:9] op_sel:[0,1]
	s_nop 0
	v_pk_fma_f32 v[8:9], v[32:33], v[0:1], v[6:7] op_sel:[0,1,1] op_sel_hi:[1,1,0] neg_lo:[0,0,1] neg_hi:[0,0,1]
	v_pk_fma_f32 v[0:1], v[32:33], v[0:1], v[6:7] op_sel:[0,1,1] op_sel_hi:[1,1,0]
	s_nop 0
	v_cvt_pk_f16_f32 v5, v8, v1
	v_pk_mul_f32 v[0:1], v[26:27], v[10:11] op_sel_hi:[1,0]
	s_nop 0
	v_pk_fma_f32 v[6:7], v[26:27], v[2:3], v[0:1] op_sel:[0,0,1] op_sel_hi:[1,1,0] neg_lo:[0,0,1] neg_hi:[0,0,1]
	v_pk_fma_f32 v[0:1], v[26:27], v[2:3], v[0:1] op_sel:[0,0,1] op_sel_hi:[1,0,0]
	s_nop 0
	v_cvt_pk_f16_f32 v6, v6, v1
	v_pk_mul_f32 v[0:1], v[28:29], v[22:23] op_sel_hi:[1,0]
	s_nop 0
	v_pk_fma_f32 v[2:3], v[28:29], v[38:39], v[0:1] op_sel:[0,0,1] op_sel_hi:[1,0,0] neg_lo:[0,0,1] neg_hi:[0,0,1]
	v_pk_fma_f32 v[0:1], v[28:29], v[38:39], v[0:1] op_sel:[0,0,1] op_sel_hi:[1,0,0]
	v_cvt_pk_f16_f32 v3, v48, v49
	v_cvt_pk_f16_f32 v7, v2, v1
	v_lshl_add_u64 v[0:1], s[12:13], 0, v[24:25]
	v_lshl_add_u64 v[0:1], v[0:1], 0, v[16:17]
	v_lshl_add_u64 v[0:1], v[0:1], 0, v[138:139]
	global_store_dwordx4 v[0:1], v[4:7], off sc1
	v_lshlrev_b64 v[0:1], 18, v[18:19]
	v_lshlrev_b32_e32 v2, 7, v145
	v_lshl_add_u64 v[0:1], s[14:15], 0, v[0:1]
	v_and_b32_e32 v16, 0x3e000, v2
	v_lshl_add_u64 v[0:1], v[0:1], 0, v[16:17]
	v_lshlrev_b32_e32 v16, 4, v20
	v_lshl_add_u64 v[4:5], v[0:1], 0, v[16:17]
	v_lshlrev_b32_e32 v16, 12, v144
	v_cvt_pk_f16_f32 v2, v46, v47
	v_cvt_pk_f16_f32 v1, v72, v73
	v_cvt_pk_f16_f32 v0, v70, v71
	v_lshl_add_u64 v[4:5], v[4:5], 0, v[16:17]
	global_store_dwordx4 v[4:5], v[0:3], off sc1
	s_nop 1
	v_cvt_pk_f16_f32 v3, v36, v37
	v_cvt_pk_f16_f32 v2, v34, v35
	v_cvt_pk_f16_f32 v1, v60, v61
	v_cvt_pk_f16_f32 v0, v58, v59
	global_store_dwordx4 v[4:5], v[0:3], off offset:1024 sc1
	s_nop 1
	v_cvt_pk_f16_f32 v3, v64, v65
	v_cvt_pk_f16_f32 v2, v62, v63
	v_cvt_pk_f16_f32 v1, v14, v15
	v_cvt_pk_f16_f32 v0, v12, v13
	global_store_dwordx4 v[4:5], v[0:3], off offset:2048 sc1
	s_nop 1
	v_cvt_pk_f16_f32 v3, v52, v53
	v_cvt_pk_f16_f32 v2, v50, v51
	v_cvt_pk_f16_f32 v1, v80, v81
	v_cvt_pk_f16_f32 v0, v78, v79
	global_store_dwordx4 v[4:5], v[0:3], off offset:3072 sc1
	s_endpgm
	.p2align	8

	.amdhsa_kernel _Z9gemm_gldsILi256ELi192ELi4ELi2ELi2ELi4ELi8ELi0ELi4096ELi3072ELi1024EEvPKDF16_S1_PfPKfS4_PKiPDF16_S7_S7_
		.amdhsa_group_segment_fixed_size 114688
		.amdhsa_private_segment_fixed_size 0
		.amdhsa_kernarg_size 72
		.amdhsa_user_sgpr_count 2
		.amdhsa_user_sgpr_dispatch_ptr 0
		.amdhsa_user_sgpr_queue_ptr 0
		.amdhsa_user_sgpr_kernarg_segment_ptr 1
		.amdhsa_user_sgpr_dispatch_id 0
		.amdhsa_user_sgpr_kernarg_preload_length 0
		.amdhsa_user_sgpr_kernarg_preload_offset 0
		.amdhsa_user_sgpr_private_segment_size 0
		.amdhsa_uses_dynamic_stack 0
		.amdhsa_enable_private_segment 0
		.amdhsa_system_sgpr_workgroup_id_x 1
		.amdhsa_system_sgpr_workgroup_id_y 0
		.amdhsa_system_sgpr_workgroup_id_z 0
		.amdhsa_system_sgpr_workgroup_info 0
		.amdhsa_system_vgpr_workitem_id 0
		.amdhsa_next_free_vgpr 220
		.amdhsa_next_free_sgpr 96
		.amdhsa_accum_offset 220
		.amdhsa_reserve_vcc 0
		.amdhsa_float_round_mode_32 0
		.amdhsa_float_round_mode_16_64 0
		.amdhsa_float_denorm_mode_32 3
		.amdhsa_float_denorm_mode_16_64 3
		.amdhsa_dx10_clamp 1
		.amdhsa_ieee_mode 1
		.amdhsa_fp16_overflow 0
		.amdhsa_tg_split 0
		.amdhsa_exception_fp_ieee_invalid_op 0
		.amdhsa_exception_fp_denorm_src 0
		.amdhsa_exception_fp_ieee_div_zero 0
		.amdhsa_exception_fp_ieee_overflow 0
		.amdhsa_exception_fp_ieee_underflow 0
		.amdhsa_exception_fp_ieee_inexact 0
		.amdhsa_exception_int_div_zero 0
	.end_amdhsa_kernel

amdhsa.kernels:
  - .agpr_count:     0
    .args:
      - .actual_access:  read_only
        .address_space:  global
        .offset:         0
        .size:           8
        .value_kind:     global_buffer
      - .actual_access:  read_only
        .address_space:  global
        .offset:         8
        .size:           8
        .value_kind:     global_buffer
      - .actual_access:  read_only
        .address_space:  global
        .offset:         16
        .size:           8
        .value_kind:     global_buffer
      - .actual_access:  read_only
        .address_space:  global
        .offset:         24
        .size:           8
        .value_kind:     global_buffer
      - .actual_access:  read_only
        .address_space:  global
        .offset:         32
        .size:           8
        .value_kind:     global_buffer
      - .actual_access:  read_only
        .address_space:  global
        .offset:         40
        .size:           8
        .value_kind:     global_buffer
      - .actual_access:  write_only
        .address_space:  global
        .offset:         48
        .size:           8
        .value_kind:     global_buffer
      - .actual_access:  write_only
        .address_space:  global
        .offset:         56
        .size:           8
        .value_kind:     global_buffer
      - .actual_access:  write_only
        .address_space:  global
        .offset:         64
        .size:           8
        .value_kind:     global_buffer
      - .actual_access:  write_only
        .address_space:  global
        .offset:         72
        .size:           8
        .value_kind:     global_buffer
      - .actual_access:  write_only
        .address_space:  global
        .offset:         80
        .size:           8
        .value_kind:     global_buffer
    .group_segment_fixed_size: 16640
    .kernarg_segment_align: 8
    .kernarg_segment_size: 88
    .language:       OpenCL C
    .language_version:
      - 2
      - 0
    .max_flat_workgroup_size: 256
    .name:           _Z11prep_kernelPKfS0_S0_S0_S0_PKiPDF16_S3_S3_PyPi
    .private_segment_fixed_size: 0
    .sgpr_count:     54
    .sgpr_spill_count: 0
    .symbol:         _Z11prep_kernelPKfS0_S0_S0_S0_PKiPDF16_S3_S3_PyPi.kd
    .uniform_work_group_size: 1
    .uses_dynamic_stack: false
    .vgpr_count:     46
    .vgpr_spill_count: 0
    .wavefront_size: 64
  - .agpr_count:     0
    .args:
      - .actual_access:  read_only
        .address_space:  global
        .offset:         0
        .size:           8
        .value_kind:     global_buffer
      - .actual_access:  read_only
        .address_space:  global
        .offset:         8
        .size:           8
        .value_kind:     global_buffer
      - .actual_access:  read_only
        .address_space:  global
        .offset:         16
        .size:           8
        .value_kind:     global_buffer
      - .actual_access:  read_only
        .address_space:  global
        .offset:         24
        .size:           8
        .value_kind:     global_buffer
      - .actual_access:  read_only
        .address_space:  global
        .offset:         32
        .size:           8
        .value_kind:     global_buffer
      - .actual_access:  write_only
        .address_space:  global
        .offset:         40
        .size:           8
        .value_kind:     global_buffer
    .group_segment_fixed_size: 36864
    .kernarg_segment_align: 8
    .kernarg_segment_size: 48
    .language:       OpenCL C
    .language_version:
      - 2
      - 0
    .max_flat_workgroup_size: 256
    .name:           _Z11attn_kernelPKDF16_S0_S0_PKyPKiPDF16_
    .private_segment_fixed_size: 0
    .sgpr_count:     32
    .sgpr_spill_count: 0
    .symbol:         _Z11attn_kernelPKDF16_S0_S0_PKyPKiPDF16_.kd
    .uniform_work_group_size: 1
    .uses_dynamic_stack: false
    .vgpr_count:     124
    .vgpr_spill_count: 0
    .wavefront_size: 64
  - .agpr_count:     0
    .args:
      - .address_space:  global
        .offset:         0
        .size:           8
        .value_kind:     global_buffer
      - .address_space:  global
        .offset:         8
        .size:           8
        .value_kind:     global_buffer
      - .actual_access:  read_only
        .address_space:  global
        .offset:         16
        .size:           8
        .value_kind:     global_buffer
      - .actual_access:  read_only
        .address_space:  global
        .offset:         24
        .size:           8
        .value_kind:     global_buffer
      - .actual_access:  read_only
        .address_space:  global
        .offset:         32
        .size:           8
        .value_kind:     global_buffer
      - .actual_access:  read_only
        .address_space:  global
        .offset:         40
        .size:           8
        .value_kind:     global_buffer
      - .actual_access:  write_only
        .address_space:  global
        .offset:         48
        .size:           8
        .value_kind:     global_buffer
      - .actual_access:  write_only
        .address_space:  global
        .offset:         56
        .size:           8
        .value_kind:     global_buffer
      - .actual_access:  write_only
        .address_space:  global
        .offset:         64
        .size:           8
        .value_kind:     global_buffer
    .group_segment_fixed_size: 114688
    .kernarg_segment_align: 8
    .kernarg_segment_size: 72
    .language:       OpenCL C
    .language_version:
      - 2
      - 0
    .max_flat_workgroup_size: 512
    .name:           _Z9gemm_gldsILi256ELi192ELi4ELi2ELi2ELi4ELi8ELi0ELi4096ELi3072ELi1024EEvPKDF16_S1_PfPKfS4_PKiPDF16_S7_S7_
    .private_segment_fixed_size: 0
    .sgpr_count:     29
    .sgpr_spill_count: 0
    .symbol:         _Z9gemm_gldsILi256ELi192ELi4ELi2ELi2ELi4ELi8ELi0ELi4096ELi3072ELi1024EEvPKDF16_S1_PfPKfS4_PKiPDF16_S7_S7_.kd
    .uniform_work_group_size: 1
    .uses_dynamic_stack: false
    .vgpr_count:     220
    .vgpr_spill_count: 0
    .wavefront_size: 64
  - .agpr_count:     0
    .args:
      - .address_space:  global
        .offset:         0
        .size:           8
        .value_kind:     global_buffer
      - .address_space:  global
        .offset:         8
        .size:           8
        .value_kind:     global_buffer
      - .actual_access:  write_only
        .address_space:  global
        .offset:         16
        .size:           8
        .value_kind:     global_buffer
      - .actual_access:  read_only
        .address_space:  global
        .offset:         24
        .size:           8
        .value_kind:     global_buffer
      - .actual_access:  read_only
        .address_space:  global
        .offset:         32
        .size:           8
        .value_kind:     global_buffer
      - .actual_access:  read_only
        .address_space:  global
        .offset:         40
        .size:           8
        .value_kind:     global_buffer
      - .actual_access:  read_only
        .address_space:  global
        .offset:         48
        .size:           8
        .value_kind:     global_buffer
      - .actual_access:  read_only
        .address_space:  global
        .offset:         56
        .size:           8
        .value_kind:     global_buffer
      - .actual_access:  read_only
        .address_space:  global
        .offset:         64
        .size:           8
        .value_kind:     global_buffer
    .group_segment_fixed_size: 98304
    .kernarg_segment_align: 8
    .kernarg_segment_size: 72
    .language:       OpenCL C
    .language_version:
      - 2
      - 0
    .max_flat_workgroup_size: 512
    .name:           _Z9gemm_gldsILi128ELi128ELi4ELi2ELi3ELi8ELi4ELi1ELi4096ELi1024ELi1024EEvPKDF16_S1_PfPKfS4_PKiPDF16_S7_S7_
    .private_segment_fixed_size: 0
    .sgpr_count:     20
    .sgpr_spill_count: 0
    .symbol:         _Z9gemm_gldsILi128ELi128ELi4ELi2ELi3ELi8ELi4ELi1ELi4096ELi1024ELi1024EEvPKDF16_S1_PfPKfS4_PKiPDF16_S7_S7_.kd
    .uniform_work_group_size: 1
    .uses_dynamic_stack: false
    .vgpr_count:     92
    .vgpr_spill_count: 0
    .wavefront_size: 64
